# P5 prologue: all 48 operand loads of the first unit issued at once (were 34 + five dependent round trips); plus P6 coefficient loads
# speedup vs baseline: 1.0069x; 1.0069x over previous
.LBB0_520:
	s_cmp_gt_i32 s78, 5
	s_cselect_b64 s[0:1], -1, 0
	s_cmp_lt_i32 s79, 6
	s_cselect_b64 s[4:5], -1, 0
	s_or_b64 s[0:1], s[0:1], s[4:5]
	s_and_b64 vcc, exec, s[0:1]
	s_cbranch_vccnz .LBB0_593
	s_lshl_b32 s0, s2, 3
	s_and_b32 s0, s0, 0xfffffc00
	s_and_b32 s1, s2, 0x7f
	v_writelane_b32 v254, s94, 8
	s_waitcnt lgkmcnt(0)
	s_or_b32 s61, s0, s1
	s_cmpk_lt_i32 s2, 0x100
	v_writelane_b32 v254, s95, 9
	v_writelane_b32 v254, s93, 10
	s_cselect_b32 s6, s61, 0x800
	v_writelane_b32 v254, s92, 11
	s_cmpk_gt_i32 s6, 0x7ff
	v_writelane_b32 v254, s91, 12
	s_cbranch_scc1 .LBB0_539
	s_add_u32 s4, s76, 0x4c5e8000
	s_addc_u32 s5, s77, 0
	s_ashr_i32 s8, s6, 10
	s_add_u32 s0, s76, 0x364e8000
	s_addc_u32 s1, s77, 0
	s_ashr_i32 s9, s8, 31
	s_lshl_b32 s3, s6, 6
	s_waitcnt vmcnt(0)
	v_lshrrev_b32_e32 v72, 3, v0
	v_mov_b32_e32 v1, 0x1ff0
	s_lshl_b64 s[8:9], s[8:9], 13
	v_bitop3_b32 v1, s3, v1, v72 bitop3:0xc8
	v_or_b32_e32 v1, s8, v1
	s_movk_i32 s3, 0x3800
	v_mov_b64_e32 v[2:3], s[0:1]
	v_and_b32_e32 v70, 0x7f, v0
	v_mad_u64_u32 v[2:3], s[10:11], v1, s3, v[2:3]
	v_mov_b32_e32 v73, 0x3800
	v_mad_i32_i24 v3, s9, v73, v3
	v_mov_b32_e32 v75, 0
	v_lshlrev_b32_e32 v74, 1, v70
	v_lshl_add_u64 v[8:9], v[2:3], 0, v[74:75]
	s_movk_i32 s7, 0x2000
	v_add_co_u32_e32 v10, vcc, s7, v8
	s_movk_i32 s7, 0x5000
	s_nop 0
	v_addc_co_u32_e32 v11, vcc, 0, v9, vcc
	v_add_co_u32_e32 v2, vcc, s7, v8
	s_mov_b32 s7, 0x9000
	s_nop 0
	v_addc_co_u32_e32 v3, vcc, 0, v9, vcc
	v_add_co_u32_e32 v14, vcc, s7, v8
	s_mov_b32 s7, 0xc000
	s_nop 0
	v_addc_co_u32_e32 v15, vcc, 0, v9, vcc
	global_load_ushort v1, v[10:11], off
	global_load_ushort v20, v[2:3], off offset:2048
	v_add_co_u32_e32 v2, vcc, s7, v8
	s_mov_b32 s7, 0x10000
	s_nop 0
	v_addc_co_u32_e32 v3, vcc, 0, v9, vcc
	v_add_co_u32_e32 v4, vcc, s7, v8
	s_mov_b32 s7, 0x13000
	s_nop 0
	v_addc_co_u32_e32 v5, vcc, 0, v9, vcc
	global_load_ushort v21, v[14:15], off
	global_load_ushort v22, v[2:3], off offset:2048
	v_add_co_u32_e32 v2, vcc, s7, v8
	s_mov_b32 s7, 0x17000
	s_nop 0
	v_addc_co_u32_e32 v3, vcc, 0, v9, vcc
	v_add_co_u32_e32 v12, vcc, s7, v8
	s_mov_b32 s7, 0x1a000
	s_nop 0
	v_addc_co_u32_e32 v13, vcc, 0, v9, vcc
	global_load_ushort v24, v[2:3], off offset:2048
	global_load_ushort v25, v[12:13], off
	v_add_co_u32_e32 v2, vcc, s7, v8
	s_mov_b32 s7, 0x1e000
	s_nop 0
	v_addc_co_u32_e32 v3, vcc, 0, v9, vcc
	global_load_ushort v50, v[2:3], off offset:2048
	v_add_co_u32_e32 v2, vcc, s7, v8
	s_mov_b32 s7, 0x21000
	s_nop 0
	v_addc_co_u32_e32 v3, vcc, 0, v9, vcc
	v_add_co_u32_e32 v6, vcc, s7, v8
	s_mov_b32 s7, 0x25000
	s_nop 0
	v_addc_co_u32_e32 v7, vcc, 0, v9, vcc
	global_load_ushort v52, v[6:7], off offset:2048
	v_add_co_u32_e32 v6, vcc, s7, v8
	s_mov_b32 s7, 0x28000
	s_nop 0
	v_addc_co_u32_e32 v7, vcc, 0, v9, vcc
	v_add_co_u32_e32 v16, vcc, s7, v8
	s_mov_b32 s7, 0x2c000
	s_nop 0
	v_addc_co_u32_e32 v17, vcc, 0, v9, vcc
	global_load_ushort v54, v[16:17], off offset:2048
	v_add_co_u32_e32 v16, vcc, s7, v8
	s_mov_b32 s7, 0x2f000
	s_nop 0
	v_addc_co_u32_e32 v17, vcc, 0, v9, vcc
	v_add_co_u32_e32 v18, vcc, s7, v8
	s_mov_b32 s7, 0x33000
	s_nop 0
	v_addc_co_u32_e32 v19, vcc, 0, v9, vcc
	global_load_ushort v56, v[18:19], off offset:2048
	v_add_co_u32_e32 v18, vcc, s7, v8
	s_mov_b32 s7, 0x36000
	s_nop 0
	v_addc_co_u32_e32 v19, vcc, 0, v9, vcc
	v_add_co_u32_e32 v26, vcc, s7, v8
	s_movk_i32 s72, 0x1000
	s_nop 0
	v_addc_co_u32_e32 v27, vcc, 0, v9, vcc
	global_load_ushort v58, v[26:27], off offset:2048
	v_add_co_u32_e32 v26, vcc, s72, v8
	s_movk_i32 s7, 0x6000
	s_nop 0
	v_addc_co_u32_e32 v27, vcc, 0, v9, vcc
	global_load_ushort v59, v[26:27], off offset:2048
	v_add_co_u32_e32 v26, vcc, s7, v8
	s_mov_b32 s7, 0x8000
	s_nop 0
	v_addc_co_u32_e32 v27, vcc, 0, v9, vcc
	v_add_co_u32_e32 v28, vcc, s7, v8
	s_mov_b32 s7, 0xd000
	s_nop 0
	v_addc_co_u32_e32 v29, vcc, 0, v9, vcc
	global_load_ushort v61, v[28:29], off offset:2048
	v_add_co_u32_e32 v28, vcc, s7, v8
	s_mov_b32 s7, 0xf000
	s_nop 0
	v_addc_co_u32_e32 v29, vcc, 0, v9, vcc
	v_add_co_u32_e32 v30, vcc, s7, v8
	s_mov_b32 s7, 0x14000
	s_nop 0
	v_addc_co_u32_e32 v31, vcc, 0, v9, vcc
	global_load_ushort v63, v[30:31], off offset:2048
	v_add_co_u32_e32 v30, vcc, s7, v8
	s_mov_b32 s7, 0x16000
	s_nop 0
	v_addc_co_u32_e32 v31, vcc, 0, v9, vcc
	v_add_co_u32_e32 v32, vcc, s7, v8
	s_mov_b32 s7, 0x1b000
	s_nop 0
	v_addc_co_u32_e32 v33, vcc, 0, v9, vcc
	global_load_ushort v65, v[32:33], off offset:2048
	v_add_co_u32_e32 v32, vcc, s7, v8
	s_mov_b32 s7, 0x1d000
	s_nop 0
	v_addc_co_u32_e32 v33, vcc, 0, v9, vcc
	v_add_co_u32_e32 v34, vcc, s7, v8
	s_mov_b32 s7, 0x22000
	s_nop 0
	v_addc_co_u32_e32 v35, vcc, 0, v9, vcc
	global_load_ushort v67, v[34:35], off offset:2048
	v_add_co_u32_e32 v34, vcc, s7, v8
	s_mov_b32 s95, 0x24000
	s_nop 0
	v_addc_co_u32_e32 v35, vcc, 0, v9, vcc
	v_add_co_u32_e32 v36, vcc, s95, v8
	s_mov_b32 s96, 0x29000
	s_nop 0
	v_addc_co_u32_e32 v37, vcc, 0, v9, vcc
	global_load_ushort v69, v[36:37], off offset:2048
	v_add_co_u32_e32 v36, vcc, s96, v8
	s_mov_b32 s97, 0x2b000
	s_nop 0
	v_addc_co_u32_e32 v37, vcc, 0, v9, vcc
	v_add_co_u32_e32 v38, vcc, s97, v8
	s_mov_b32 s34, 0x30000
	s_nop 0
	v_addc_co_u32_e32 v39, vcc, 0, v9, vcc
	global_load_ushort v93, v[38:39], off offset:2048
	v_add_co_u32_e32 v38, vcc, s34, v8
	s_mov_b32 s35, 0x32000
	s_nop 0
	v_addc_co_u32_e32 v39, vcc, 0, v9, vcc
	v_add_co_u32_e32 v40, vcc, s35, v8
	s_mov_b32 s88, 0x37000
	s_nop 0
	v_addc_co_u32_e32 v41, vcc, 0, v9, vcc
	global_load_ushort v66, v[32:33], off offset:-4096
	global_load_ushort v68, v[34:35], off offset:-4096
	global_load_ushort v92, v[36:37], off offset:-4096
	global_load_ushort v94, v[38:39], off offset:-4096
	global_load_ushort v96, v[40:41], off offset:2048
	v_add_co_u32_e32 v40, vcc, s88, v8
	global_load_ushort v23, v[4:5], off
	global_load_ushort v53, v[6:7], off
	global_load_ushort v55, v[16:17], off
	global_load_ushort v57, v[18:19], off
	global_load_ushort v60, v[26:27], off offset:-4096
	global_load_ushort v62, v[28:29], off offset:-4096
	global_load_ushort v64, v[30:31], off offset:-4096
	global_load_ushort v51, v[2:3], off
	v_addc_co_u32_e32 v41, vcc, 0, v9, vcc
	global_load_ushort v8, v[40:41], off offset:-4096
	global_load_ushort v9, v[10:11], off offset:2048
	s_nop 0
	global_load_ushort v10, v[26:27], off
	global_load_ushort v226, v[14:15], off offset:2048
	global_load_ushort v227, v[28:29], off
	global_load_ushort v228, v[4:5], off offset:2048
	global_load_ushort v229, v[30:31], off
	global_load_ushort v230, v[12:13], off offset:2048
	global_load_ushort v231, v[32:33], off
	global_load_ushort v232, v[2:3], off offset:2048
	global_load_ushort v233, v[34:35], off
	global_load_ushort v234, v[6:7], off offset:2048
	global_load_ushort v235, v[36:37], off
	global_load_ushort v236, v[16:17], off offset:2048
	global_load_ushort v237, v[38:39], off
	global_load_ushort v238, v[18:19], off offset:2048
	global_load_ushort v239, v[40:41], off
	s_ashr_i32 s7, s6, 31
	s_lshl_b64 s[6:7], s[6:7], 15
	s_add_u32 s6, s4, s6
	s_addc_u32 s7, s5, s7
	v_mov_b32_e32 v77, v75
	s_movk_i32 s86, 0x4000
	v_mov_b32_e32 v79, v75
	v_mov_b32_e32 v81, v75
	s_add_u32 s48, s76, 0x506e8000
	s_mov_b32 s12, 0xf400
	s_addc_u32 s49, s77, 0
	s_add_u32 s54, s76, 0x546e8000
	v_readlane_b32 s13, v254, 10
	s_addc_u32 s55, s77, 0
	s_bfe_u32 s20, s13, 0x20006
	v_readlane_b32 s31, v254, 12
	s_movk_i32 s29, 0x110
	s_lshr_b32 s21, s13, 7
	s_and_b32 s22, s21, 0x1fffffe
	s_movk_i32 s28, 0x90
	s_mov_b32 s73, 0x5040100
	s_movk_i32 s8, 0x17f
	s_movk_i32 s10, 0x1ff
	s_waitcnt vmcnt(46)
	v_perm_b32 v160, v20, v1, s73
	v_mov_b32_e32 v1, 0x8487b800
	s_mov_b32 s66, 0x3a800000
	v_and_b32_e32 v71, 48, v72
	s_mov_b32 s43, 0
	v_cmp_lt_u32_e64 s[8:9], s8, v0
	v_cmp_lt_u32_e64 s[10:11], s10, v0
	s_waitcnt vmcnt(44)
	v_perm_b32 v159, v22, v21, s73
	s_waitcnt vmcnt(41)
	v_perm_b32 v157, v50, v25, s73
	s_movk_i32 s74, 0xd800
	s_brev_b32 s67, 60
	s_mov_b32 s75, 0x800000
	s_mov_b32 s89, 0x42fe0000
	s_mov_b32 s90, 0x40c0c00
	v_mov_b32_e32 v131, 0x8a88b000
	s_mov_b32 s91, 0
	v_mov_b32_e32 v133, v75
	v_mov_b32_e32 v135, v75
	v_mov_b32_e32 v137, v75
	v_mov_b32_e32 v139, v75
	v_mov_b32_e32 v141, v75
	v_mov_b32_e32 v143, v75
	v_mov_b32_e32 v145, v75
	v_mov_b32_e32 v147, v75
	v_mov_b32_e32 v132, v75
	v_mov_b32_e32 v134, v75
	v_mov_b32_e32 v136, v75
	v_mov_b32_e32 v138, v75
	v_mov_b32_e32 v140, v75
	v_mov_b32_e32 v142, v75
	v_mov_b32_e32 v144, v75
	v_mov_b32_e32 v146, v75
	s_waitcnt vmcnt(29)
	v_perm_b32 v149, v66, v65, s73
	s_waitcnt vmcnt(28)
	v_perm_b32 v148, v68, v67, s73
	s_waitcnt vmcnt(27)
	v_perm_b32 v69, v92, v69, s73
	s_waitcnt vmcnt(26)
	v_perm_b32 v68, v94, v93, s73
	v_lshl_or_b32 v92, v190, 3, v1
	v_mov_b32_e32 v93, v75
	v_lshlrev_b32_e32 v94, 4, v190
	s_waitcnt vmcnt(24)
	v_perm_b32 v158, v24, v23, s73
	s_waitcnt vmcnt(23)
	v_perm_b32 v155, v54, v53, s73
	s_waitcnt vmcnt(22)
	v_perm_b32 v154, v56, v55, s73
	s_waitcnt vmcnt(21)
	v_perm_b32 v153, v58, v57, s73
	s_waitcnt vmcnt(20)
	v_perm_b32 v152, v60, v59, s73
	s_waitcnt vmcnt(19)
	v_perm_b32 v151, v62, v61, s73
	s_waitcnt vmcnt(18)
	v_perm_b32 v150, v64, v63, s73
	s_waitcnt vmcnt(17)
	v_perm_b32 v156, v52, v51, s73
	s_waitcnt vmcnt(16)
	v_perm_b32 v67, v8, v96, s73
	v_mov_b32_e32 v1, v75
	s_waitcnt vmcnt(14)
	v_lshl_or_b32 v26, v10, 16, v9
	s_nop 0
	s_nop 0
	v_mov_b32_e32 v8, v75
	s_waitcnt vmcnt(12)
	v_lshl_or_b32 v27, v227, 16, v226
	s_waitcnt vmcnt(10)
	v_lshl_or_b32 v28, v229, 16, v228
	s_nop 0
	s_nop 0
	v_lshlrev_b32_e32 v9, 4, v0
	v_and_b32_e32 v74, 0xf0, v9
	v_and_b32_e32 v76, 0x1f00, v9
	v_add_u32_e32 v13, 0, v74
	v_lshl_add_u64 v[82:83], s[4:5], 0, v[74:75]
	s_lshl_b32 s4, s31, 4
	s_and_b32 s42, s4, 0x3fffffc0
	s_or_b32 s64, s4, 48
	s_add_i32 s4, 0, 0x17c00
	s_cmp_le_u32 s22, s20
	s_cselect_b64 s[56:57], -1, 0
	s_lshl_b32 s87, s22, 5
	s_or_b32 s30, s21, 1
	v_and_b32_e32 v10, 0x70, v9
	v_lshl_add_u32 v85, v0, 2, s4
	v_lshl_add_u32 v87, v70, 2, s4
	s_movk_i32 s4, 0x80
	v_cmp_gt_u32_e64 s[4:5], s4, v0
	s_waitcnt vmcnt(8)
	v_lshl_or_b32 v29, v231, 16, v230
	s_waitcnt vmcnt(6)
	v_lshl_or_b32 v30, v233, 16, v232
	v_mov_b32_e32 v6, 0x2000
	s_waitcnt vmcnt(4)
	v_lshl_or_b32 v31, v235, 16, v234
	s_waitcnt vmcnt(2)
	v_lshl_or_b32 v32, v237, 16, v236
	s_waitcnt vmcnt(0)
	v_lshl_or_b32 v33, v239, 16, v238
	v_lshl_add_u64 v[2:3], s[6:7], 0, v[74:75]
	v_lshl_add_u64 v[4:5], v[2:3], 0, v[76:77]
	global_load_dwordx4 v[34:37], v[4:5], off
	v_add_co_u32_e32 v4, vcc, s86, v4
	s_movk_i32 s6, 0x3f00
	s_nop 0
	v_addc_co_u32_e32 v5, vcc, 0, v5, vcc
	v_bitop3_b32 v78, v9, s6, v6 bitop3:0xc8
	global_load_dwordx4 v[42:45], v[4:5], off
	s_movk_i32 s6, 0x7f00
	v_mov_b32_e32 v4, 0x6000
	v_bitop3_b32 v80, v9, s6, v4 bitop3:0xc8
	v_lshl_add_u64 v[6:7], v[2:3], 0, v[78:79]
	v_lshl_add_u64 v[2:3], v[2:3], 0, v[80:81]
	global_load_dwordx4 v[38:41], v[6:7], off
	global_load_dwordx4 v[46:49], v[2:3], off
	v_lshrrev_b32_e32 v4, 7, v0
	v_mul_u32_u24_e32 v5, 0x880, v4
	v_lshlrev_b32_e32 v11, 5, v4
	v_lshrrev_b32_e32 v4, 4, v0
	v_mul_u32_u24_e32 v4, 0x110, v4
	v_add3_u32 v95, v13, v4, s12
	v_or_b32_e32 v4, 0x200, v0
	v_lshrrev_b32_e32 v4, 4, v4
	v_and_b32_e32 v2, 15, v0
	v_mul_u32_u24_e32 v14, 0x110, v4
	v_or_b32_e32 v4, 0x600, v0
	v_lshrrev_b32_e32 v3, 4, v190
	v_lshl_or_b32 v84, s20, 4, v2
	v_lshrrev_b32_e32 v4, 4, v4
	v_lshlrev_b32_e32 v12, 2, v3
	v_mul_u32_u24_e32 v15, 0x110, v4
	v_lshlrev_b32_e32 v99, 3, v3
	v_and_b32_e32 v3, 48, v190
	v_mad_u32_u24 v4, v84, s29, 0
	v_add_u32_e32 v16, 0, v3
	v_add_u32_e32 v109, v4, v3
	v_lshlrev_b32_e32 v3, 7, v84
	v_sub_u32_e32 v3, v4, v3
	s_lshl_b32 s12, s22, 4
	v_add_u32_e32 v114, v3, v99
	v_or_b32_e32 v3, s12, v2
	v_mul_lo_u32 v17, v3, s29
	v_or_b32_e32 v3, s12, v12
	s_cmp_le_u32 s30, s20
	v_cmp_gt_u32_e64 s[12:13], v3, v84
	v_cmp_lt_u32_e64 s[14:15], v3, v84
	v_or_b32_e32 v4, 2, v3
	v_or_b32_e32 v3, 3, v3
	s_cselect_b64 s[58:59], -1, 0
	s_lshl_b32 s20, s30, 4
	v_cmp_gt_u32_e64 s[18:19], v3, v84
	v_or_b32_e32 v3, s20, v2
	v_mul_lo_u32 v18, v3, s29
	v_or_b32_e32 v3, s20, v12
	v_cmp_gt_u32_e64 s[16:17], v4, v84
	v_cmp_gt_u32_e64 s[20:21], v3, v84
	v_cmp_lt_u32_e64 s[22:23], v3, v84
	v_or_b32_e32 v4, 2, v3
	v_or_b32_e32 v3, 3, v3
	v_or_b32_e32 v5, v5, v70
	v_cmp_gt_u32_e64 s[26:27], v3, v84
	s_lshl_b32 s70, s30, 5
	v_or_b32_e32 v3, s42, v2
	s_add_i32 s30, 0, 0x18400
	v_lshl_add_u32 v89, v5, 1, 0
	v_mad_u32_u24 v9, v70, s28, 0
	v_cmp_gt_u32_e64 s[24:25], v4, v84
	v_or_b32_e32 v4, 16, v3
	v_or_b32_e32 v5, 32, v3
	v_or_b32_e32 v2, s64, v2
	v_lshl_add_u32 v115, v84, 3, s30
	s_and_b32 s30, s31, 0x3fffffc
	v_lshlrev_b32_e32 v74, 2, v10
	s_movk_i32 s6, 0xff
	v_mul_lo_u32 v19, v3, s28
	v_mul_lo_u32 v97, v4, s28
	v_mul_lo_u32 v98, v5, s28
	v_mul_lo_u32 v100, v2, s28
	v_mul_lo_u32 v101, v3, s29
	v_mul_lo_u32 v102, v4, s29
	v_mul_lo_u32 v103, v5, s29
	v_mul_lo_u32 v104, v2, s29
	v_lshl_add_u64 v[90:91], s[36:37], 0, v[74:75]
	s_add_u32 s36, s76, 0x8688b000
	v_add_u32_e32 v117, v9, v11
	v_mbcnt_lo_u32_b32 v9, -1, 0
	v_cmp_lt_u32_e64 s[6:7], s6, v0
	v_cmp_gt_u32_e64 s[28:29], 16, v190
	v_add_u32_e32 v116, s30, v115
	v_or_b32_e32 v86, s42, v12
	v_or_b32_e32 v88, s64, v12
	s_addc_u32 s37, s77, 0
	s_lshl_b32 s71, s31, 3
	v_cmp_eq_u32_e64 s[30:31], 0, v190
	v_mov_b32_e32 v2, v75
	v_mov_b32_e32 v4, v75
	v_mov_b32_e32 v3, v75
	v_mov_b32_e32 v6, v75
	v_mov_b32_e32 v5, v75
	v_mov_b32_e32 v7, v75
	v_lshlrev_b32_e32 v74, 1, v10
	v_lshlrev_b32_e32 v96, 1, v12
	s_lshl_b32 s60, s42, 1
	s_lshl_b32 s64, s64, 1
	v_add_u32_e32 v118, v13, v14
	v_add_u32_e32 v119, v13, v15
	v_add_u32_e32 v120, v16, v17
	v_add_u32_e32 v121, v16, v18
	v_add_u32_e32 v122, v16, v19
	v_add_u32_e32 v123, v16, v97
	v_add_u32_e32 v124, v16, v98
	v_add_u32_e32 v125, v16, v100
	v_add_u32_e32 v126, v16, v101
	v_add_u32_e32 v127, v16, v102
	v_add_u32_e32 v128, v16, v103
	v_add_u32_e32 v129, v16, v104
	v_mbcnt_hi_u32_b32 v130, -1, v9
	v_mov_b32_e32 v98, 0x358637bd
	s_branch .LBB0_524
